# baseline (speedup 1.0000x reference)
.LBB0_283:
	s_or_b64 exec, exec, s[0:1]
	s_waitcnt vmcnt(2)
	v_lshrrev_b32_e32 v4, 4, v160
	s_lshl_b32 s0, s78, 5
	v_or_b32_e32 v165, s0, v4
	v_mov_b32_e32 v4, 0x24400
	s_add_i32 s69, s33, 33
	v_lshl_or_b32 v169, v72, 2, v4
	v_mul_u32_u24_e32 v4, 10, v160
	s_cmp_gt_i32 s77, 8
	s_cselect_b64 s[18:19], -1, 0
	s_cmp_gt_i32 s77, 10
	v_lshlrev_b32_e32 v12, 2, v4
	v_mov_b32_e32 v13, 0
	v_or_b32_e32 v164, 0x100, v160
	v_cvt_f64_f32_e32 v[10:11], v5
	v_mov_b32_e32 v5, 0x10000
	s_cselect_b64 s[20:21], -1, 0
	s_cmp_gt_i32 s77, 12
	v_lshl_add_u64 v[14:15], s[48:49], 0, v[12:13]
	v_lshlrev_b32_e32 v4, 9, v70
	v_lshlrev_b32_e32 v12, 2, v70
	v_lshl_or_b32 v67, v160, 2, v5
	v_lshl_or_b32 v69, v164, 2, v5
	s_cselect_b64 s[22:23], -1, 0
	v_add3_u32 v172, v4, s3, v75
	v_lshl_add_u64 v[4:5], s[60:61], 0, v[12:13]
	s_add_i32 s24, s24, s3
	v_lshl_add_u64 v[40:41], v[4:5], 0, 64
	v_add_u32_e32 v4, s24, v75
	v_mov_b32_e32 v5, v13
	v_lshlrev_b64 v[4:5], 11, v[4:5]
	s_waitcnt vmcnt(1)
	v_cmp_gt_f32_e32 vcc, 0, v161
	v_or_b32_e32 v4, v4, v12
	v_lshrrev_b32_e32 v6, 4, v164
	v_cndmask_b32_e64 v167, 0, 1.0, vcc
	s_waitcnt vmcnt(0)
	v_cmp_gt_f32_e32 vcc, 0, v162
	s_mov_b64 s[10:11], 0x2800
	s_lshl_b32 s70, s68, 16
	v_lshl_add_u64 v[4:5], s[72:73], 0, v[4:5]
	v_mov_b32_e32 v12, v13
	s_mov_b32 s26, 0x3f7d73e7
	s_mov_b32 s28, 0xa37fcc69
	s_mov_b32 s34, 0x3f779b79
	s_mov_b32 s36, 0x3d064869
	v_or_b32_e32 v166, s0, v6
	v_cndmask_b32_e64 v168, 0, 1.0, vcc
	v_cmp_gt_u32_e64 s[0:1], 32, v73
	v_lshl_add_u32 v170, v73, 5, s33
	v_lshl_add_u64 v[34:35], v[14:15], 0, s[10:11]
	s_bitset1_b32 s70, 21
	v_lshlrev_b32_e32 v171, 3, v70
	v_lshl_add_u64 v[42:43], v[4:5], 0, 64
	s_mov_b64 s[38:39], 0
	v_mov_b64_e32 v[44:45], 0
	s_mov_b64 s[24:25], 0
	s_mov_b32 s27, 0x3d8414e8
	s_mov_b32 s29, 0x3fee7078
	s_mov_b32 s3, 0xf000
	s_mov_b64 s[30:31], 0x80
	s_mov_b32 s35, 0x3f7383c5
	s_mov_b32 s37, 0x3d47c3ae
	s_mov_b32 s71, 0xffff
	v_mov_b32_e32 v47, 0x3f6f7d63
	v_bfrev_b32_e32 v173, 1
	v_mov_b32_e32 v174, 0x2f0
	v_mov_b32_e32 v175, 0x26c10
	s_mov_b64 s[40:41], 0
	s_mov_b64 s[44:45], 0
	v_mov_b32_e32 v176, 0
	v_mov_b64_e32 v[36:37], 0
	v_mov_b64_e32 v[6:7], 0
	v_mov_b64_e32 v[48:49], 0
	v_mov_b64_e32 v[38:39], 0
	v_mov_b64_e32 v[4:5], 0
	v_mov_b32_e32 v177, 0
	v_mov_b64_e32 v[50:51], v[12:13]
	v_mov_b64_e32 v[56:57], v[12:13]
	v_mov_b64_e32 v[52:53], v[12:13]
	v_mov_b64_e32 v[58:59], v[12:13]
	v_mov_b32_e32 v54, v13
	v_mov_b32_e32 v55, v13
	v_mul_f32_e32 v218, v9, v18
	v_mul_f32_e32 v219, v131, v19
	v_mul_f32_e32 v220, v134, v20
	v_mul_f32_e32 v221, v137, v21
	v_mul_f32_e32 v222, v140, v22
	v_mul_f32_e32 v223, v143, v23
	v_mul_f32_e32 v224, v146, v24
	v_mul_f32_e32 v225, v150, v25
	v_mul_f32_e32 v226, v121, v26
	v_mul_f32_e32 v227, v122, v27
	v_mov_b32_e32 v250, 0
	v_add_u16_e32 v208, v250, v159
	v_add_u16_e32 v209, v250, v158
	v_add_u16_e32 v210, v250, v157
	v_add_u16_e32 v211, v250, v156
	v_add_u16_e32 v212, v250, v155
	v_add_u16_e32 v213, v250, v154
	v_add_u16_e32 v214, v250, v153
	v_add_u16_e32 v215, v250, v149
	v_add_u16_e32 v216, v250, v128
	v_add_u16_e32 v217, v250, v127
	s_mov_b64 s[86:87], 0
	s_and_saveexec_b64 s[82:83], s[42:43]
	v_lshlrev_b32_e32 v208, 7, v165
	v_lshlrev_b32_e32 v210, 7, v166
	v_mov_b32_e32 v209, 0x100000
	v_mov_b32_e32 v211, 0x100000
	s_mov_b64 exec, s[82:83]
	s_branch .LBB0_288

.Lmy_rd8:
	ds_read_b64 v[228:229], v208
	ds_read_b64 v[230:231], v209
	ds_read_b64 v[232:233], v210
	ds_read_b64 v[234:235], v211
	ds_read_b64 v[236:237], v212
	ds_read_b64 v[238:239], v213
	ds_read_b64 v[240:241], v214
	ds_read_b64 v[242:243], v215
	s_waitcnt lgkmcnt(7)
	v_fma_f32 v180, v228, v218, 0
	s_waitcnt lgkmcnt(6)
	v_fmac_f32_e32 v180, v230, v219
	v_mul_f32_e32 v250, v129, v229
	v_cmp_class_f32_e64 s[82:83], v228, 64
	s_waitcnt lgkmcnt(5)
	v_fmac_f32_e32 v180, v232, v220
	v_mul_f32_e32 v251, v132, v231
	v_cmp_class_f32_e64 s[84:85], v230, 64
	s_waitcnt lgkmcnt(4)
	v_fmac_f32_e32 v180, v234, v221
	v_fma_f32 v18, v250, v54, v18
	v_fma_f32 v19, v251, v54, v19
	s_waitcnt lgkmcnt(3)
	v_fmac_f32_e32 v180, v236, v222
	v_cndmask_b32_e64 v250, -v130, v173, s[82:83]
	v_cndmask_b32_e64 v251, -v133, v173, s[84:85]
	s_waitcnt lgkmcnt(2)
	v_fmac_f32_e32 v180, v238, v223
	v_fmac_f32_e32 v18, v250, v55
	v_fmac_f32_e32 v19, v251, v55
	s_waitcnt lgkmcnt(1)
	v_fmac_f32_e32 v180, v240, v224
	v_med3_f32 v18, v18, v71, 0
	v_med3_f32 v19, v19, v81, 0
	s_waitcnt lgkmcnt(0)
	v_fmac_f32_e32 v180, v242, v225
	v_mul_f32_e32 v218, v9, v18
	v_mul_f32_e32 v219, v131, v19
	s_cbranch_vccnz .LBB0_318
	v_fmac_f32_e32 v180, v244, v226
	v_fmac_f32_e32 v180, v246, v227
	s_andn2_b64 vcc, exec, s[20:21]
	s_cbranch_vccnz .LBB0_318
	v_and_b32_e32 v12, 0xf000, v181
	v_add_u16_e32 v46, v12, v120
	ds_read_b64 v[60:61], v46
	v_add_u16_e32 v46, v12, v119
	ds_read_b64 v[62:63], v46
	v_mul_f32_e32 v64, v112, v28
	s_andn2_b64 vcc, exec, s[22:23]
	s_waitcnt lgkmcnt(1)
	v_mul_f32_e32 v46, v115, v61
	v_cmp_class_f32_e64 s[58:59], v60, 64
	v_fma_f32 v28, v46, v54, v28
	v_fmac_f32_e32 v180, v60, v64
	v_cndmask_b32_e64 v46, -v117, v173, s[58:59]
	v_fmac_f32_e32 v28, v46, v55
	v_mul_f32_e32 v46, v113, v29
	s_waitcnt lgkmcnt(0)
	v_fmac_f32_e32 v180, v62, v46
	v_mul_f32_e32 v46, v116, v63
	v_cmp_class_f32_e64 s[58:59], v62, 64
	v_fma_f32 v29, v46, v54, v29
	v_med3_f32 v28, v28, v93, 0
	v_cndmask_b32_e64 v46, -v118, v173, s[58:59]
	v_fmac_f32_e32 v29, v46, v55
	v_med3_f32 v29, v29, v94, 0
	s_cbranch_vccnz .LBB0_318
	v_add_u16_e32 v46, v12, v114
	v_add_u16_e32 v62, v12, v111
	v_add_u16_e32 v64, v12, v17
	v_add_u16_e32 v12, v12, v8
	ds_read_b64 v[60:61], v46
	ds_read_b64 v[62:63], v62
	ds_read_b64 v[64:65], v64
	ds_read_b64 v[72:73], v12
	v_mul_f32_e32 v12, v100, v30
	s_waitcnt lgkmcnt(3)
	v_fmac_f32_e32 v180, v60, v12
	v_mul_f32_e32 v12, v103, v61
	v_cmp_class_f32_e64 s[58:59], v60, 64
	v_fma_f32 v12, v12, v54, v30
	s_nop 0
	v_cndmask_b32_e64 v30, -v107, v173, s[58:59]
	v_fmac_f32_e32 v12, v30, v55
	v_med3_f32 v30, v12, v95, 0
	v_mul_f32_e32 v12, v101, v31
	s_waitcnt lgkmcnt(2)
	v_fmac_f32_e32 v180, v62, v12
	v_mul_f32_e32 v12, v104, v63
	v_cmp_class_f32_e64 s[58:59], v62, 64
	v_fma_f32 v12, v12, v54, v31
	s_nop 0
	v_cndmask_b32_e64 v31, -v108, v173, s[58:59]
	v_fmac_f32_e32 v12, v31, v55
	v_med3_f32 v31, v12, v96, 0
	v_mul_f32_e32 v12, v102, v32
	s_waitcnt lgkmcnt(1)
	v_fmac_f32_e32 v180, v64, v12
	v_mul_f32_e32 v12, v105, v65
	v_cmp_class_f32_e64 s[58:59], v64, 64
	v_fma_f32 v12, v12, v54, v32
	s_nop 0
	v_cndmask_b32_e64 v32, -v109, v173, s[58:59]
	v_fmac_f32_e32 v12, v32, v55
	v_med3_f32 v32, v12, v97, 0
	v_mul_f32_e32 v12, v16, v33
	s_waitcnt lgkmcnt(0)
	v_fmac_f32_e32 v180, v72, v12
	v_mul_f32_e32 v12, v106, v73
	v_cmp_class_f32_e64 s[58:59], v72, 64
	v_fmac_f32_e32 v33, v12, v54
	s_nop 0
	v_cndmask_b32_e64 v12, -v110, v173, s[58:59]
	v_fmac_f32_e32 v33, v12, v55
	v_med3_f32 v33, v33, v99, 0
.LBB0_318:
	v_mul_f32_e32 v250, v135, v233
	v_cmp_class_f32_e64 s[82:83], v232, 64
	v_add_f32_dpp v12, v180, v180 row_ror:8 row_mask:0xf bank_mask:0xf bound_ctrl:1
	v_mov_b32_e32 v61, v13
	v_cndmask_b32_e64 v46, v176, 5, s[16:17]
	v_mul_f32_e32 v251, v138, v235
	v_cmp_class_f32_e64 s[84:85], v234, 64
	v_add_f32_dpp v12, v12, v12 row_ror:4 row_mask:0xf bank_mask:0xf bound_ctrl:1
	s_mov_b64 s[60:61], s[16:17]
	v_fma_f32 v20, v250, v54, v20
	v_fma_f32 v21, v251, v54, v21
	v_cndmask_b32_e64 v250, -v136, v173, s[82:83]
	v_add_f32_dpp v60, v12, v12 row_ror:2 row_mask:0xf bank_mask:0xf bound_ctrl:1
	v_mov_b32_e32 v12, 48
	v_cndmask_b32_e64 v251, -v139, v173, s[84:85]
	v_fmac_f32_e32 v20, v250, v55
	v_fmac_f32_e32 v21, v251, v55
	v_mov_b32_dpp v61, v60 row_ror:1 row_mask:0xf bank_mask:0xf
	s_and_saveexec_b64 s[58:59], s[10:11]
	s_cbranch_execz .LBB0_286
	v_med3_f32 v20, v20, v85, 0
	v_med3_f32 v21, v21, v86, 0
	v_add_f32_e32 v12, v60, v61
	v_cvt_f64_f32_e32 v[248:249], v12
	v_mul_f32_e32 v220, v134, v20
	v_mul_f32_e32 v221, v137, v21
	v_mul_f32_e32 v250, v141, v237
	v_fmac_f64_e32 v[248:249], v[0:1], v[10:11]
	v_cmp_gt_i32_e32 vcc, 1, v46
	v_mov_b32_e32 v12, 0
	v_cmp_class_f32_e64 s[82:83], v236, 64
	v_mul_f32_e32 v251, v144, v239
	v_cmp_class_f32_e64 s[84:85], v238, 64
	v_fma_f32 v22, v250, v54, v22
	v_cndmask_b32_e32 v1, 0, v249, vcc
	v_cndmask_b32_e32 v0, 0, v248, vcc
	s_waitcnt lgkmcnt(0)
	v_cvt_f64_f32_e32 v[248:249], v179
	v_fma_f32 v23, v251, v54, v23
	v_cndmask_b32_e64 v250, -v142, v173, s[82:83]
	v_cndmask_b32_e64 v251, -v145, v173, s[84:85]
	v_add_f64 v[0:1], v[0:1], v[248:249]
	v_fmac_f32_e32 v22, v250, v55
	v_fmac_f32_e32 v23, v251, v55
	v_med3_f32 v22, v22, v87, 0
	v_med3_f32 v23, v23, v88, 0
	v_cmp_le_f64_e32 vcc, 1.0, v[0:1]
	v_mul_f32_e32 v222, v140, v22
	v_mul_f32_e32 v223, v143, v23
	v_mul_f32_e32 v250, v147, v241
	v_cmp_class_f32_e64 s[82:83], v240, 64
	s_lshr_b32 s11, vcc_lo, 15
	s_and_b32 s10, vcc_lo, 1
	s_and_b32 s11, s11, 2
	s_or_b32 s60, s11, s10
	s_lshr_b64 s[10:11], vcc, 30
	s_and_b32 s10, s10, 4
	s_lshr_b32 s11, vcc_hi, 13
	s_or_b32 s10, s60, s10
	s_and_b32 s11, s11, 8
	s_or_b32 s10, s10, s11
	v_lshlrev_b32_e64 v248, v163, s10
	s_and_saveexec_b64 s[10:11], s[4:5]
	v_and_b32_e32 v12, 3, v178
	v_lshl_or_b32 v12, v12, 2, v175
	v_or_b32_e32 v249, 0x10000, v248
	ds_add_rtn_u32 v12, v12, v249
	s_or_b64 exec, exec, s[10:11]
	v_mul_f32_e32 v251, v151, v243
	v_cmp_class_f32_e64 s[84:85], v242, 64
	v_fma_f32 v24, v250, v54, v24
	v_fma_f32 v25, v251, v54, v25
	v_cndmask_b32_e64 v250, -v148, v173, s[82:83]
	v_cndmask_b32_e64 v251, -v152, v173, s[84:85]
	v_fmac_f32_e32 v24, v250, v55
	v_fmac_f32_e32 v25, v251, v55
	v_med3_f32 v24, v24, v89, 0
	v_med3_f32 v25, v25, v90, 0
	v_mul_f32_e32 v224, v146, v24
	v_mul_f32_e32 v225, v150, v25
	v_add_u16_e32 v208, 0x1000, v208
	v_add_u16_e32 v209, 0x1000, v209
	v_add_u16_e32 v210, 0x1000, v210
	v_add_u16_e32 v211, 0x1000, v211
	v_add_u16_e32 v212, 0x1000, v212
	v_add_u16_e32 v213, 0x1000, v213
	v_add_u16_e32 v214, 0x1000, v214
	v_add_u16_e32 v215, 0x1000, v215
	s_cmp_eq_u64 s[18:19], 0
	s_cbranch_scc1 .Lmy_no89
	v_mul_f32_e32 v250, v123, v245
	v_cmp_class_f32_e64 s[82:83], v244, 64
	v_mul_f32_e32 v251, v124, v247
	v_cmp_class_f32_e64 s[84:85], v246, 64
	v_fma_f32 v26, v250, v54, v26
	v_fma_f32 v27, v251, v54, v27
	v_cndmask_b32_e64 v250, -v125, v173, s[82:83]
	v_cndmask_b32_e64 v251, -v126, v173, s[84:85]
	v_fmac_f32_e32 v26, v250, v55
	v_fmac_f32_e32 v27, v251, v55
	v_med3_f32 v26, v26, v91, 0
	v_med3_f32 v27, v27, v92, 0
	v_mul_f32_e32 v226, v121, v26
	v_mul_f32_e32 v227, v122, v27
	v_add_u16_e32 v216, 0x1000, v216
	v_add_u16_e32 v217, 0x1000, v217
